# v052 + out-proj (attention and gMLP) tile-loop head drains turned into counted waits
# baseline (speedup 1.0000x reference)
.LBB0_419:
	s_lshl_b32 s30, s23, 6
	s_add_u32 s52, s6, 0x37e00000
	s_addc_u32 s53, s7, 0
	s_add_u32 s6, s4, 0x80
	s_addc_u32 s7, s5, 0
	s_add_i32 s31, s15, 0x18000
	v_mov_b32_e32 v4, v149
	s_waitcnt vmcnt(2)
	s_barrier
	s_mov_b32 m0, s31
	s_mov_b32 s66, 0
	global_load_lds_dwordx4 v4, s[6:7]
	s_add_u32 s6, s4, 0x20080
	s_addc_u32 s7, s5, 0
	v_mov_b32_e32 v4, v149
	s_add_i32 s34, s15, 0x1a000
	s_mov_b32 m0, s34
	v_add_u32_e32 v150, 0, v3
	global_load_lds_dwordx4 v4, s[6:7]
	s_add_u32 s6, s0, 0x80
	s_addc_u32 s7, s1, 0
	v_mov_b32_e32 v4, v148
	s_add_i32 s35, s15, 0x8000
	s_mov_b32 m0, s35
	v_add_u32_e32 v151, 0, v2
	global_load_lds_dwordx4 v4, s[6:7]
	s_add_u32 s6, s0, 0x10080
	s_addc_u32 s7, s1, 0
	v_mov_b32_e32 v4, v148
	s_add_i32 s36, s15, 0xa000
	s_mov_b32 m0, s36
	s_add_i32 s37, s15, 0x1c000
	global_load_lds_dwordx4 v4, s[6:7]
	s_add_u32 s6, s4, 0x8080
	s_addc_u32 s7, s5, 0
	v_mov_b32_e32 v4, v149
	s_mov_b32 m0, s37
	v_readlane_b32 s42, v255, 5
	global_load_lds_dwordx4 v4, s[6:7]
	s_add_u32 s6, s4, 0x28080
	s_addc_u32 s7, s5, 0
	s_add_i32 s64, s15, 0x1e000
	v_mov_b32_e32 v4, v149
	s_mov_b32 m0, s64
	s_cmpk_lt_u32 s8, 0x100
	global_load_lds_dwordx4 v4, s[6:7]
	s_waitcnt vmcnt(0)
	v_readlane_b32 s6, v255, 18
	s_cselect_b64 s[54:55], -1, 0
	s_lshl_b32 s65, s9, 6
	s_mov_b32 s23, s6
	s_barrier
	v_readlane_b32 s7, v255, 19
	s_branch .LBB0_422

.LBB0_428:
	s_ashr_i32 s59, s58, 31
	s_lshl_b64 s[6:7], s[58:59], 18
	s_add_u32 s60, s10, s6
	s_addc_u32 s61, s12, s7
	s_and_b64 s[6:7], s[40:41], exec
	s_cselect_b32 s43, s61, s1
	s_cselect_b32 s59, s60, s0
	s_ashr_i32 s57, s56, 31
	s_lshl_b64 s[6:7], s[56:57], 18
	s_add_u32 s62, s13, s6
	s_addc_u32 s63, s14, s7
	s_and_b64 s[6:7], s[40:41], exec
	s_cselect_b32 s57, s63, s5
	s_cselect_b32 s67, s62, s4
	s_add_u32 s0, s0, 0x20080
	s_addc_u32 s1, s1, 0
	s_add_u32 s68, s4, 0x100
	v_mov_b32_e32 v2, 0
	s_addc_u32 s69, s5, 0
	s_mov_b32 s70, -2
	v_mov_b32_e32 v3, v2
	v_mov_b32_e32 v4, v2
	v_mov_b32_e32 v5, v2
	v_mov_b32_e32 v6, v2
	v_mov_b32_e32 v7, v2
	v_mov_b32_e32 v8, v2
	v_mov_b32_e32 v9, v2
	v_mov_b32_e32 v18, v2
	v_mov_b32_e32 v19, v2
	v_mov_b32_e32 v20, v2
	v_mov_b32_e32 v21, v2
	v_mov_b32_e32 v22, v2
	v_mov_b32_e32 v23, v2
	v_mov_b32_e32 v24, v2
	v_mov_b32_e32 v25, v2
	v_mov_b32_e32 v34, v2
	v_mov_b32_e32 v35, v2
	v_mov_b32_e32 v36, v2
	v_mov_b32_e32 v37, v2
	v_mov_b32_e32 v38, v2
	v_mov_b32_e32 v39, v2
	v_mov_b32_e32 v40, v2
	v_mov_b32_e32 v41, v2
	v_mov_b32_e32 v50, v2
	v_mov_b32_e32 v51, v2
	v_mov_b32_e32 v52, v2
	v_mov_b32_e32 v53, v2
	v_mov_b32_e32 v54, v2
	v_mov_b32_e32 v55, v2
	v_mov_b32_e32 v56, v2
	v_mov_b32_e32 v57, v2
	v_mov_b32_e32 v10, v2
	v_mov_b32_e32 v11, v2
	v_mov_b32_e32 v12, v2
	v_mov_b32_e32 v13, v2
	s_waitcnt vmcnt(2)
	v_mov_b32_e32 v14, v2
	v_mov_b32_e32 v15, v2
	v_mov_b32_e32 v16, v2
	v_mov_b32_e32 v17, v2
	v_mov_b32_e32 v26, v2
	v_mov_b32_e32 v27, v2
	v_mov_b32_e32 v28, v2
	v_mov_b32_e32 v29, v2
	v_mov_b32_e32 v30, v2
	v_mov_b32_e32 v31, v2
	v_mov_b32_e32 v32, v2
	v_mov_b32_e32 v33, v2
	v_mov_b32_e32 v42, v2
	v_mov_b32_e32 v43, v2
	v_mov_b32_e32 v44, v2
	v_mov_b32_e32 v45, v2
	v_mov_b32_e32 v46, v2
	v_mov_b32_e32 v47, v2
	v_mov_b32_e32 v48, v2
	v_mov_b32_e32 v49, v2
	v_mov_b32_e32 v58, v2
	v_mov_b32_e32 v59, v2
	v_mov_b32_e32 v60, v2
	v_mov_b32_e32 v61, v2
	v_mov_b32_e32 v62, v2
	v_mov_b32_e32 v63, v2
	v_mov_b32_e32 v64, v2
	v_mov_b32_e32 v65, v2
	v_mov_b32_e32 v66, v2
	v_mov_b32_e32 v67, v2
	v_mov_b32_e32 v68, v2
	v_mov_b32_e32 v69, v2
	v_mov_b32_e32 v70, v2
	v_mov_b32_e32 v71, v2
	v_mov_b32_e32 v72, v2
	v_mov_b32_e32 v73, v2
	v_mov_b32_e32 v82, v2
	v_mov_b32_e32 v83, v2
	v_mov_b32_e32 v84, v2
	v_mov_b32_e32 v85, v2
	v_mov_b32_e32 v86, v2
	v_mov_b32_e32 v87, v2
	v_mov_b32_e32 v88, v2
	v_mov_b32_e32 v89, v2
	v_mov_b32_e32 v98, v2
	v_mov_b32_e32 v99, v2
	v_mov_b32_e32 v100, v2
	v_mov_b32_e32 v101, v2
	v_mov_b32_e32 v102, v2
	v_mov_b32_e32 v103, v2
	v_mov_b32_e32 v104, v2
	v_mov_b32_e32 v105, v2
	v_mov_b32_e32 v114, v2
	v_mov_b32_e32 v115, v2
	v_mov_b32_e32 v116, v2
	v_mov_b32_e32 v117, v2
	v_mov_b32_e32 v118, v2
	v_mov_b32_e32 v119, v2
	v_mov_b32_e32 v120, v2
	v_mov_b32_e32 v121, v2
	v_mov_b32_e32 v74, v2
	v_mov_b32_e32 v75, v2
	v_mov_b32_e32 v76, v2
	v_mov_b32_e32 v77, v2
	v_mov_b32_e32 v78, v2
	v_mov_b32_e32 v79, v2
	v_mov_b32_e32 v80, v2
	v_mov_b32_e32 v81, v2
	v_mov_b32_e32 v90, v2
	v_mov_b32_e32 v91, v2
	v_mov_b32_e32 v92, v2
	v_mov_b32_e32 v93, v2
	v_mov_b32_e32 v94, v2
	v_mov_b32_e32 v95, v2
	v_mov_b32_e32 v96, v2
	v_mov_b32_e32 v97, v2
	v_mov_b32_e32 v106, v2
	v_mov_b32_e32 v107, v2
	v_mov_b32_e32 v108, v2
	v_mov_b32_e32 v109, v2
	v_mov_b32_e32 v110, v2
	v_mov_b32_e32 v111, v2
	v_mov_b32_e32 v112, v2
	v_mov_b32_e32 v113, v2
	v_mov_b32_e32 v122, v2
	v_mov_b32_e32 v123, v2
	v_mov_b32_e32 v124, v2
	v_mov_b32_e32 v125, v2
	v_mov_b32_e32 v126, v2
	v_mov_b32_e32 v127, v2
	v_mov_b32_e32 v128, v2
	v_mov_b32_e32 v129, v2

.LBB0_763:
	s_lshl_b32 s31, s31, 6
	s_lshl_b32 s10, s28, 10
	s_add_u32 s50, s8, 0x37e00000
	s_addc_u32 s51, s9, 0
	s_lshl_b64 s[8:9], s[10:11], 2
	s_waitcnt lgkmcnt(0)
	s_add_u32 s52, s6, s8
	s_addc_u32 s53, s7, s9
	s_add_u32 s8, s4, 0x80
	s_addc_u32 s9, s5, 0
	s_add_i32 s10, s16, 0x18000
	v_mov_b32_e32 v4, v157
	s_waitcnt vmcnt(2)
	s_barrier
	s_mov_b32 m0, s10
	s_mov_b32 s71, s11
	global_load_lds_dwordx4 v4, s[8:9]
	s_add_u32 s8, s4, 0xc0080
	s_addc_u32 s9, s5, 0
	v_mov_b32_e32 v4, v157
	s_add_i32 s28, s16, 0x1a000
	s_mov_b32 m0, s28
	s_mov_b32 s63, 0
	global_load_lds_dwordx4 v4, s[8:9]
	s_add_u32 s8, s0, 0x80
	s_addc_u32 s9, s1, 0
	v_mov_b32_e32 v4, v156
	s_add_i32 s34, s16, 0x8000
	s_mov_b32 m0, s34
	v_add_u32_e32 v158, 0, v3
	global_load_lds_dwordx4 v4, s[8:9]
	s_add_u32 s8, s0, 0x60080
	s_addc_u32 s9, s1, 0
	v_mov_b32_e32 v4, v156
	s_add_i32 s35, s16, 0xa000
	s_mov_b32 m0, s35
	s_add_i32 s36, s16, 0x1c000
	global_load_lds_dwordx4 v4, s[8:9]
	s_add_u32 s8, s4, 0x30080
	s_addc_u32 s9, s5, 0
	v_mov_b32_e32 v4, v157
	s_mov_b32 m0, s36
	v_add_u32_e32 v159, 0, v2
	global_load_lds_dwordx4 v4, s[8:9]
	s_add_u32 s8, s4, 0xf0080
	s_addc_u32 s9, s5, 0
	s_add_i32 s37, s16, 0x1e000
	v_mov_b32_e32 v4, v157
	s_mov_b32 m0, s37
	s_cmpk_lt_u32 s23, 0x100
	global_load_lds_dwordx4 v4, s[8:9]
	s_waitcnt vmcnt(0)
	s_cselect_b64 s[54:55], -1, 0
	s_lshl_b32 s62, s38, 6
	s_cmp_lg_u64 s[6:7], 0
	v_readlane_b32 s6, v255, 18
	s_cselect_b64 s[56:57], -1, 0
	v_readlane_b32 s66, v255, 5
	s_mov_b32 s23, s6
	s_barrier
	v_readlane_b32 s7, v255, 19
	s_branch .LBB0_766

.LBB0_776:
	s_add_u32 s0, s0, 0xc0080
	s_addc_u32 s1, s1, 0
	s_add_u32 s40, s4, 0x100
	v_mov_b32_e32 v2, 0
	s_addc_u32 s41, s5, 0
	s_mov_b32 s67, -2
	v_mov_b32_e32 v3, v2
	v_mov_b32_e32 v4, v2
	v_mov_b32_e32 v5, v2
	v_mov_b32_e32 v6, v2
	v_mov_b32_e32 v7, v2
	v_mov_b32_e32 v8, v2
	v_mov_b32_e32 v9, v2
	v_mov_b32_e32 v18, v2
	v_mov_b32_e32 v19, v2
	v_mov_b32_e32 v20, v2
	v_mov_b32_e32 v21, v2
	v_mov_b32_e32 v22, v2
	v_mov_b32_e32 v23, v2
	v_mov_b32_e32 v24, v2
	v_mov_b32_e32 v25, v2
	v_mov_b32_e32 v34, v2
	v_mov_b32_e32 v35, v2
	v_mov_b32_e32 v36, v2
	v_mov_b32_e32 v37, v2
	v_mov_b32_e32 v38, v2
	v_mov_b32_e32 v39, v2
	v_mov_b32_e32 v40, v2
	v_mov_b32_e32 v41, v2
	v_mov_b32_e32 v50, v2
	v_mov_b32_e32 v51, v2
	v_mov_b32_e32 v52, v2
	v_mov_b32_e32 v53, v2
	v_mov_b32_e32 v58, v2
	v_mov_b32_e32 v59, v2
	v_mov_b32_e32 v60, v2
	v_mov_b32_e32 v61, v2
	v_mov_b32_e32 v10, v2
	v_mov_b32_e32 v11, v2
	v_mov_b32_e32 v12, v2
	v_mov_b32_e32 v13, v2
	s_waitcnt vmcnt(2)
	v_mov_b32_e32 v14, v2
	v_mov_b32_e32 v15, v2
	v_mov_b32_e32 v16, v2
	v_mov_b32_e32 v17, v2
	v_mov_b32_e32 v26, v2
	v_mov_b32_e32 v27, v2
	v_mov_b32_e32 v28, v2
	v_mov_b32_e32 v29, v2
	v_mov_b32_e32 v30, v2
	v_mov_b32_e32 v31, v2
	v_mov_b32_e32 v32, v2
	v_mov_b32_e32 v33, v2
	v_mov_b32_e32 v42, v2
	v_mov_b32_e32 v43, v2
	v_mov_b32_e32 v44, v2
	v_mov_b32_e32 v45, v2
	v_mov_b32_e32 v46, v2
	v_mov_b32_e32 v47, v2
	v_mov_b32_e32 v48, v2
	v_mov_b32_e32 v49, v2
	v_mov_b32_e32 v62, v2
	v_mov_b32_e32 v63, v2
	v_mov_b32_e32 v64, v2
	v_mov_b32_e32 v65, v2
	v_mov_b32_e32 v70, v2
	v_mov_b32_e32 v71, v2
	v_mov_b32_e32 v72, v2
	v_mov_b32_e32 v73, v2
	v_mov_b32_e32 v74, v2
	v_mov_b32_e32 v75, v2
	v_mov_b32_e32 v76, v2
	v_mov_b32_e32 v77, v2
	v_mov_b32_e32 v78, v2
	v_mov_b32_e32 v79, v2
	v_mov_b32_e32 v80, v2
	v_mov_b32_e32 v81, v2
	v_mov_b32_e32 v90, v2
	v_mov_b32_e32 v91, v2
	v_mov_b32_e32 v92, v2
	v_mov_b32_e32 v93, v2
	v_mov_b32_e32 v94, v2
	v_mov_b32_e32 v95, v2
	v_mov_b32_e32 v96, v2
	v_mov_b32_e32 v97, v2
	v_mov_b32_e32 v106, v2
	v_mov_b32_e32 v107, v2
	v_mov_b32_e32 v108, v2
	v_mov_b32_e32 v109, v2
	v_mov_b32_e32 v110, v2
	v_mov_b32_e32 v111, v2
	v_mov_b32_e32 v112, v2
	v_mov_b32_e32 v113, v2
	v_mov_b32_e32 v122, v2
	v_mov_b32_e32 v123, v2
	v_mov_b32_e32 v124, v2
	v_mov_b32_e32 v125, v2
	v_mov_b32_e32 v126, v2
	v_mov_b32_e32 v127, v2
	v_mov_b32_e32 v128, v2
	v_mov_b32_e32 v129, v2
	v_mov_b32_e32 v82, v2
	v_mov_b32_e32 v83, v2
	v_mov_b32_e32 v84, v2
	v_mov_b32_e32 v85, v2
	v_mov_b32_e32 v86, v2
	v_mov_b32_e32 v87, v2
	v_mov_b32_e32 v88, v2
	v_mov_b32_e32 v89, v2
	v_mov_b32_e32 v98, v2
	v_mov_b32_e32 v99, v2
	v_mov_b32_e32 v100, v2
	v_mov_b32_e32 v101, v2
	v_mov_b32_e32 v102, v2
	v_mov_b32_e32 v103, v2
	v_mov_b32_e32 v104, v2
	v_mov_b32_e32 v105, v2
	v_mov_b32_e32 v114, v2
	v_mov_b32_e32 v115, v2
	v_mov_b32_e32 v116, v2
	v_mov_b32_e32 v117, v2
	v_mov_b32_e32 v118, v2
	v_mov_b32_e32 v119, v2
	v_mov_b32_e32 v120, v2
	v_mov_b32_e32 v121, v2
	v_mov_b32_e32 v130, v2
	v_mov_b32_e32 v131, v2
	v_mov_b32_e32 v132, v2
	v_mov_b32_e32 v133, v2
	v_mov_b32_e32 v134, v2
	v_mov_b32_e32 v135, v2
	v_mov_b32_e32 v136, v2
	v_mov_b32_e32 v137, v2
